# P0 rebalance: helper CUs convert x rows [0,12288), transposing CUs the last 4096 (was all rows on helpers)
# baseline (speedup 1.0000x reference)
.LBB0_898:
	s_lshl_b32 s8, s43, 3
	s_add_i32 s8, s8, s91
	s_lshl_b32 s10, s42, 3
	s_movk_i32 s99, 0x3fff
	s_cmp_lg_u32 s42, 0x100
	s_cbranch_scc1 .Lp0_xs_done
	s_and_b32 s98, s43, 31
	s_lshr_b32 s8, s43, 5
	s_cmp_lt_u32 s98, 8
	s_cbranch_scc1 .Lp0_xs_B
	s_mul_i32 s8, s8, 24
	s_add_i32 s8, s8, s98
	s_add_i32 s8, s8, -8
	s_lshl_b32 s8, s8, 3
	s_add_i32 s8, s8, s91
	s_addk_i32 s8, 0x3000
	s_movk_i32 s10, 0x600
	s_branch .Lp0_xs_done
.Lp0_xs_B:
	s_mul_i32 s8, s8, 8
	s_add_i32 s8, s8, s98
	s_lshl_b32 s8, s8, 3
	s_add_i32 s8, s8, s91
	s_movk_i32 s10, 0x200
	s_movk_i32 s99, 0x2fff
